# baseline (speedup 1.0000x reference)
_Z11attn_kernelPKDF16_S0_S0_PfPDF16_S1_:
	v_and_b32_e32 v65, 63, v0
	s_lshl_b32 s3, s2, 7
	s_lshr_b32 s4, s2, 2
	s_and_b32 s3, s3, 0x180
	s_and_b32 s4, s4, 0x3ffffffe
	s_add_i32 s3, s3, s4
	s_bfe_u32 s2, s2, 0x10002
	s_or_b32 s40, s3, s2
	s_mov_b32 s41, 0
	s_lshl_b64 s[2:3], s[40:41], 2
	s_getpc_b64 s[4:5]
	s_add_u32 s4, s4, g_tab@rel32@lo+4
	s_addc_u32 s5, s5, g_tab@rel32@hi+12
	s_add_u32 s42, s4, s2
	s_addc_u32 s43, s5, s3
	s_load_dword s12, s[42:43], 0x0
	s_load_dwordx4 s[4:7], s[0:1], 0x8
	s_load_dword s76, s[42:43], 0x1000
	s_load_dwordx2 s[80:81], s[0:1], 0x0
	s_load_dwordx4 s[84:87], s[0:1], 0x18
	s_load_dwordx2 s[88:89], s[0:1], 0x28
	v_lshlrev_b32_e32 v2, 4, v0
	s_movk_i32 s8, 0x70
	v_readfirstlane_b32 s3, v0
	s_waitcnt lgkmcnt(0)
	s_add_u32 s70, s4, 0x2000
	s_addc_u32 s71, s5, 0
	s_add_u32 s72, s6, 0x2000
	s_addc_u32 s73, s7, 0
	s_and_b32 s2, s12, 3
	s_lshl_b32 s10, s2, 19
	v_bitop3_b32 v10, v2, s8, v0 bitop3:0x48
	s_add_u32 s8, s6, s10
	s_addc_u32 s9, s7, 0
	s_lshr_b32 s13, s3, 6
	s_bfe_u32 s40, s12, 0x70007
	s_bfe_u32 s33, s12, 0x6000e
	v_and_b32_e32 v1, 0x1f80, v2
	s_add_u32 s10, s4, s10
	v_or_b32_e32 v50, v10, v1
	v_mov_b32_e32 v51, 0
	s_addc_u32 s11, s5, 0
	v_lshl_add_u64 v[52:53], s[10:11], 0, v[50:51]
	v_lshl_add_u64 v[54:55], s[8:9], 0, v[50:51]
	s_lshl_b32 s8, s40, 13
	s_mov_b32 s9, s41
	s_lshl_b32 s50, s13, 10
	v_lshl_add_u64 v[2:3], v[52:53], 0, s[8:9]
	s_mov_b32 m0, s50
	s_add_i32 s51, s50, 0x2000
	global_load_lds_dwordx4 v[2:3], off
	v_lshl_add_u64 v[2:3], v[54:55], 0, s[8:9]
	s_mov_b32 m0, s51
	s_cmp_eq_u32 s33, 0
	global_load_lds_dwordx4 v[2:3], off
	s_cbranch_scc1 .LBB2_30
	s_mov_b64 s[14:15], s[80:81]
	s_mov_b64 s[8:9], s[84:85]
	s_mov_b64 s[10:11], s[86:87]
	s_mov_b64 s[44:45], s[88:89]
	s_lshl_b32 s52, s13, 4
	s_lshl_b32 s0, s2, 12
	v_and_b32_e32 v56, 15, v0
	v_bfe_u32 v15, v0, 4, 2
	v_lshrrev_b32_e32 v14, 1, v0
	v_bfe_u32 v2, v0, 1, 3
	s_add_i32 s54, s52, s0
	v_lshlrev_b32_e32 v16, 7, v56
	v_bitop3_b32 v3, v15, v14, 7 bitop3:0x78
	v_bitop3_b32 v2, v15, v2, 4 bitop3:0x36
	s_bfe_u32 s53, s12, 0x50002
	v_or_b32_e32 v18, s54, v56
	v_lshl_or_b32 v57, v3, 4, v16
	v_lshl_or_b32 v81, v2, 4, v16
	v_lshl_add_u32 v2, s53, 7, v18
	v_mov_b32_e32 v3, v51
	v_lshlrev_b64 v[2:3], 7, v[2:3]
	v_and_b32_e32 v50, 48, v0
	s_waitcnt lgkmcnt(0)
	v_lshl_add_u64 v[2:3], s[14:15], 0, v[2:3]
	v_lshl_add_u64 v[12:13], v[2:3], 0, v[50:51]
	global_load_dwordx4 v[2:5], v[12:13], off offset:64
	global_load_dwordx4 v[6:9], v[12:13], off
	v_and_b32_e32 v11, 63, v0
	v_bfe_u32 v12, v0, 5, 1
	s_mulk_i32 s13, 0xc00
	v_and_b32_e32 v13, 7, v0
	v_cmp_gt_u32_e64 s[0:1], 16, v11
	v_bitop3_b32 v11, v12, v0, 7 bitop3:0x78
	s_lshr_b32 s55, s3, 8
	s_add_i32 s3, s50, s13
	v_and_b32_e32 v14, 8, v14
	v_lshlrev_b32_e32 v23, 4, v11
	v_bitop3_b32 v11, v12, v13, 2 bitop3:0x36
	v_add3_u32 v19, s3, v16, v14
	v_bfe_u32 v14, v0, 3, 3
	v_lshlrev_b32_e32 v24, 4, v11
	v_bitop3_b32 v11, v12, v13, 4 bitop3:0x36
	v_bitop3_b32 v16, v14, v0, 7 bitop3:0x78
	v_lshlrev_b32_e32 v25, 4, v11
	v_bitop3_b32 v11, v12, v13, 6 bitop3:0x36
	v_bitop3_b32 v0, v15, v0, 15 bitop3:0x78
	v_lshl_add_u64 v[58:59], s[14:15], 0, v[50:51]
	v_lshlrev_b32_e32 v50, 4, v13
	v_lshlrev_b32_e32 v13, 4, v11
	v_or_b32_e32 v11, 8, v14
	v_lshlrev_b32_e32 v86, 4, v0
	v_bitop3_b32 v0, v15, v56, 4 bitop3:0x36
	v_or_b32_e32 v17, 4, v15
	v_lshl_add_u32 v21, v16, 4, s3
	v_lshlrev_b32_e32 v26, 7, v14
	v_lshlrev_b32_e32 v12, 6, v14
	v_lshlrev_b32_e32 v27, 7, v11
	v_lshlrev_b32_e32 v14, 6, v11
	v_lshlrev_b32_e32 v87, 4, v0
	v_or_b32_e32 v0, 8, v15
	v_bitop3_b32 v11, v15, v56, 8 bitop3:0x36
	v_bitop3_b32 v16, v15, v56, 12 bitop3:0x36
	v_lshlrev_b32_e32 v83, 2, v15
	v_add_u32_e32 v84, 0x80, v18
	v_lshl_add_u64 v[60:61], s[10:11], 0, v[50:51]
	v_lshlrev_b32_e32 v50, 4, v56
	v_lshlrev_b32_e32 v88, 4, v11
	v_or_b32_e32 v11, 12, v15
	v_lshlrev_b32_e32 v89, 4, v16
	v_lshl_add_u32 v28, v15, 8, s3
	v_lshlrev_b32_e32 v16, 6, v15
	v_lshl_add_u32 v15, v17, 8, s3
	v_lshlrev_b32_e32 v18, 6, v17
	v_lshl_add_u32 v17, v0, 8, s3
	v_lshlrev_b32_e32 v20, 6, v0
	v_add_u32_e32 v0, v1, v10
	v_lshl_add_u64 v[62:63], s[8:9], 0, v[50:51]
	s_lshl_b32 s8, s53, 1
	v_lshl_or_b32 v50, s2, 19, v0
	s_mov_b64 s[46:47], 0x2000
	v_lshl_add_u32 v85, v56, 8, s3
	v_lshl_add_u32 v29, v11, 8, s3
	v_lshlrev_b32_e32 v22, 6, v11
	s_add_i32 s3, s55, s8
	v_lshl_add_u64 v[10:11], v[50:51], 0, s[46:47]
	v_or_b32_e32 v82, s52, v56
	s_add_i32 s56, s8, 2
	s_sub_i32 s57, 0, s3
	v_lshl_add_u64 v[0:1], s[4:5], 0, v[10:11]
	s_and_b32 s78, s50, 0xc00
	s_lshl_b32 s78, s78, 1
	v_lshrrev_b32_e32 v77, 3, v65
	v_lshrrev_b32_e32 v78, 4, v65
	v_and_b32_e32 v79, 7, v65
	v_xor_b32_e32 v78, v79, v78
	v_lshlrev_b32_e32 v78, 4, v78
	v_lshl_add_u32 v77, v77, 7, v78
	v_add_u32_e32 v77, s78, v77
	v_lshl_or_b32 v64, s2, 19, v77
	v_add_u32_e32 v65, 0x400, v64
	v_xor_b32_e32 v65, 64, v65
	s_mov_b32 s58, 0x40c00000
	s_mov_b32 s36, 0x3c003c00
	v_mov_b32_e32 v116, s36
	v_mov_b32_e32 v117, s36
	v_mov_b32_e32 v118, s36
	v_mov_b32_e32 v119, s36
	v_add_u32_e32 v90, v19, v23
	v_add_u32_e32 v91, v19, v24
	v_add_u32_e32 v92, v19, v25
	v_add_u32_e32 v93, v19, v13
	v_add_u32_e32 v94, v21, v26
	v_lshlrev_b32_e32 v50, 1, v12
	v_add_u32_e32 v95, v21, v27
	v_lshlrev_b32_e32 v66, 1, v14
	v_add_u32_e32 v96, v28, v86
	v_lshlrev_b32_e32 v68, 2, v16
	v_add_u32_e32 v97, v15, v87
	v_lshlrev_b32_e32 v70, 2, v18
	v_add_u32_e32 v98, v17, v88
	v_lshlrev_b32_e32 v72, 2, v20
	v_add_u32_e32 v99, v29, v89
	v_lshlrev_b32_e32 v74, 2, v22
	v_mov_b32_e32 v100, 0xff800000
	v_mov_b32_e32 v101, 0xf149f2ca
	s_mov_b32 s59, s41
	s_branch .LBB2_3
